# GQA QK^T K-slice reads triple-buffered (prefetch distance 2 slices) in the two in-loop sections, on top of v63
# baseline (speedup 1.0000x reference)
.LBB0_846:
	ds_read_b128 v[64:67], v177 offset:49152
	ds_read_b128 v[68:71], v177 offset:57344
	ds_read_b128 v[188:191], v178 offset:49152
	ds_read_b128 v[204:207], v178 offset:57344
	ds_read_b128 v[230:233], v179 offset:49152
	ds_read_b128 v[234:237], v179 offset:57344
	ds_read_b128 v[238:241], v180 offset:49152
	ds_read_b128 v[242:245], v180 offset:57344
	v_add_f32_e32 v187, 0, v202
	v_add_f32_e32 v187, v221, v187
	s_waitcnt lgkmcnt(7)
	v_mfma_f32_32x32x16_bf16 v[80:95], v[64:67], v[126:129], 0
	v_add_f32_e32 v187, v222, v187
	v_add_f32_e32 v187, v223, v187
	v_add_f32_e32 v187, v224, v187
	v_add_f32_e32 v187, v225, v187
	v_add_f32_e32 v187, v201, v187
	v_add_f32_e32 v187, v203, v187
	v_add_f32_e32 v187, v196, v187
	s_waitcnt lgkmcnt(6)
	v_mfma_f32_32x32x16_bf16 v[64:79], v[68:71], v[126:129], 0
	v_add_f32_e32 v187, v198, v187
	v_add_f32_e32 v187, v199, v187
	v_add_f32_e32 v187, v200, v187
	v_exp_f32_e32 v142, v142
	v_add_f32_e32 v187, v193, v187
	v_exp_f32_e32 v143, v143
	v_add_f32_e32 v187, v194, v187
	s_waitcnt lgkmcnt(5)
	v_mfma_f32_32x32x16_bf16 v[80:95], v[188:191], v[122:125], v[80:95]
	v_exp_f32_e32 v140, v140
	v_add_f32_e32 v187, v195, v187
	v_exp_f32_e32 v141, v141
	v_add_f32_e32 v187, v197, v187
	v_exp_f32_e32 v134, v134
	v_add_f32_e32 v187, v142, v187
	v_exp_f32_e32 v135, v135
	s_waitcnt lgkmcnt(4)
	v_mfma_f32_32x32x16_bf16 v[64:79], v[204:207], v[122:125], v[64:79]
	ds_read_b128 v[188:191], v181 offset:49152
	ds_read_b128 v[204:207], v181 offset:57344
	v_add_f32_e32 v187, v143, v187
	v_exp_f32_e32 v132, v132
	v_add_f32_e32 v187, v140, v187
	v_exp_f32_e32 v133, v133
	v_add_f32_e32 v187, v141, v187
	v_exp_f32_e32 v130, v130
	s_waitcnt lgkmcnt(5)
	v_mfma_f32_32x32x16_bf16 v[80:95], v[230:233], v[118:121], v[80:95]
	v_add_f32_e32 v187, v134, v187
	v_exp_f32_e32 v131, v131
	v_add_f32_e32 v187, v135, v187
	v_exp_f32_e32 v144, v144
	v_add_f32_e32 v187, v132, v187
	v_exp_f32_e32 v145, v145
	v_add_f32_e32 v187, v133, v187
	s_waitcnt lgkmcnt(4)
	v_mfma_f32_32x32x16_bf16 v[64:79], v[234:237], v[118:121], v[64:79]
	ds_read_b128 v[230:233], v182 offset:49152
	ds_read_b128 v[234:237], v182 offset:57344
	v_exp_f32_e32 v138, v138
	v_add_f32_e32 v187, v130, v187
	v_exp_f32_e32 v139, v139
	v_add_f32_e32 v187, v131, v187
	v_exp_f32_e32 v136, v136
	v_add_f32_e32 v187, v144, v187
	s_waitcnt lgkmcnt(5)
	v_mfma_f32_32x32x16_bf16 v[80:95], v[238:241], v[114:117], v[80:95]
	v_exp_f32_e32 v137, v137
	v_add_f32_e32 v187, v145, v187
	v_add_f32_e32 v187, v138, v187
	v_add_f32_e32 v187, v139, v187
	v_add_f32_e32 v187, v136, v187
	v_add_f32_e32 v187, v137, v187
	v_cvt_pk_bf16_f32 v192, v193, v194
	s_waitcnt lgkmcnt(4)
	v_mfma_f32_32x32x16_bf16 v[64:79], v[242:245], v[114:117], v[64:79]
	ds_read_b128 v[238:241], v183 offset:49152
	ds_read_b128 v[242:245], v183 offset:57344
	v_cvt_pk_bf16_f32 v193, v195, v197
	v_cvt_pk_bf16_f32 v194, v142, v143
	v_cvt_pk_bf16_f32 v195, v140, v141
	v_cvt_pk_bf16_f32 v197, v132, v133
	s_nop 1
	v_permlane32_swap_b32_e32 v195, v197
	s_waitcnt lgkmcnt(5)
	v_mfma_f32_32x32x16_bf16 v[80:95], v[188:191], v[110:113], v[80:95]
	s_waitcnt lgkmcnt(4)
	v_mfma_f32_32x32x16_bf16 v[64:79], v[204:207], v[110:113], v[64:79]
	ds_read_b128 v[188:191], v184 offset:49152
	ds_read_b128 v[204:207], v184 offset:57344
	s_waitcnt lgkmcnt(5)
	v_mfma_f32_32x32x16_bf16 v[80:95], v[230:233], v[106:109], v[80:95]
	s_waitcnt lgkmcnt(4)
	v_mfma_f32_32x32x16_bf16 v[64:79], v[234:237], v[106:109], v[64:79]
	s_waitcnt lgkmcnt(3)
	v_mfma_f32_32x32x16_bf16 v[80:95], v[238:241], v[102:105], v[80:95]
	s_waitcnt lgkmcnt(2)
	v_mfma_f32_32x32x16_bf16 v[64:79], v[242:245], v[102:105], v[64:79]
	s_waitcnt lgkmcnt(1)
	v_mfma_f32_32x32x16_bf16 v[80:95], v[188:191], v[98:101], v[80:95]
	v_mov_b32_e32 v188, v187
	v_cvt_pk_bf16_f32 v190, v196, v198
	s_nop 0
	v_permlane32_swap_b32_e32 v187, v188
	v_cvt_pk_bf16_f32 v191, v199, v200
	v_permlane32_swap_b32_e32 v190, v192
	s_waitcnt lgkmcnt(0)
	v_mfma_f32_32x32x16_bf16 v[64:79], v[204:207], v[98:101], v[64:79]
	v_cvt_pk_bf16_f32 v204, v202, v221
	v_cvt_pk_bf16_f32 v205, v222, v223
	v_cvt_pk_bf16_f32 v206, v224, v225
	v_cvt_pk_bf16_f32 v207, v201, v203
	v_cvt_pk_bf16_f32 v196, v134, v135
	v_cvt_pk_bf16_f32 v198, v130, v131
	v_cvt_pk_bf16_f32 v199, v144, v145
	v_cvt_pk_bf16_f32 v200, v138, v139
	v_cvt_pk_bf16_f32 v201, v136, v137
	v_permlane32_swap_b32_e32 v204, v206
	v_permlane32_swap_b32_e32 v205, v207
	v_permlane32_swap_b32_e32 v191, v193
	v_permlane32_swap_b32_e32 v194, v196
	v_permlane32_swap_b32_e32 v198, v200
	v_permlane32_swap_b32_e32 v199, v201
	v_add_co_u32_e32 v138, vcc, s65, v166
	s_nop 1
	v_addc_co_u32_e32 v139, vcc, 0, v167, vcc
	global_load_dwordx4 v[130:133], v[166:167], off offset:512
	global_load_dwordx4 v[134:137], v[166:167], off
	global_load_dwordx4 v[142:145], v[138:139], off offset:512
	s_nop 0
	global_load_dwordx4 v[138:141], v[138:139], off
	ds_read_b64_tr_b16 v[208:209], v169 offset:0
	ds_read_b64_tr_b16 v[210:211], v169 offset:0x800
	ds_read_b64_tr_b16 v[212:213], v169 offset:0x1000
	ds_read_b64_tr_b16 v[214:215], v169 offset:0x1800
	ds_read_b64_tr_b16 v[218:219], v169 offset:0x2000
	ds_read_b64_tr_b16 v[220:221], v169 offset:0x2800
	ds_read_b64_tr_b16 v[222:223], v169 offset:0x3000
	ds_read_b64_tr_b16 v[224:225], v169 offset:0x3800
	s_waitcnt lgkmcnt(0)
	s_nop 0
	v_mfma_f32_32x32x16_bf16 v[0:15], v[204:207], v[208:211], v[0:15]
	ds_read_b64_tr_b16 v[208:209], v169 offset:0x200
	ds_read_b64_tr_b16 v[210:211], v169 offset:0xa00
	v_mfma_f32_32x32x16_bf16 v[0:15], v[190:193], v[212:215], v[0:15]
	ds_read_b64_tr_b16 v[212:213], v169 offset:0x1200
	ds_read_b64_tr_b16 v[214:215], v169 offset:0x1a00
	v_mfma_f32_32x32x16_bf16 v[0:15], v[194:197], v[218:221], v[0:15]
	ds_read_b64_tr_b16 v[218:219], v169 offset:0x2200
	ds_read_b64_tr_b16 v[220:221], v169 offset:0x2a00
	v_mfma_f32_32x32x16_bf16 v[0:15], v[198:201], v[222:225], v[0:15]
	ds_read_b64_tr_b16 v[222:223], v169 offset:0x3200
	ds_read_b64_tr_b16 v[224:225], v169 offset:0x3a00
	s_waitcnt lgkmcnt(0)
	v_mfma_f32_32x32x16_bf16 v[48:63], v[204:207], v[208:211], v[48:63]
	ds_read_b64_tr_b16 v[208:209], v169 offset:0x400
	ds_read_b64_tr_b16 v[210:211], v169 offset:0xc00
	v_mfma_f32_32x32x16_bf16 v[48:63], v[190:193], v[212:215], v[48:63]
	ds_read_b64_tr_b16 v[212:213], v169 offset:0x1400
	ds_read_b64_tr_b16 v[214:215], v169 offset:0x1c00
	v_mfma_f32_32x32x16_bf16 v[48:63], v[194:197], v[218:221], v[48:63]
	ds_read_b64_tr_b16 v[218:219], v169 offset:0x2400
	ds_read_b64_tr_b16 v[220:221], v169 offset:0x2c00
	v_mfma_f32_32x32x16_bf16 v[48:63], v[198:201], v[222:225], v[48:63]
	ds_read_b64_tr_b16 v[222:223], v169 offset:0x3400
	ds_read_b64_tr_b16 v[224:225], v169 offset:0x3c00
	s_waitcnt lgkmcnt(0)
	v_mfma_f32_32x32x16_bf16 v[32:47], v[204:207], v[208:211], v[32:47]
	ds_read_b64_tr_b16 v[208:209], v169 offset:0x600
	ds_read_b64_tr_b16 v[210:211], v169 offset:0xe00
	v_mfma_f32_32x32x16_bf16 v[32:47], v[190:193], v[212:215], v[32:47]
	ds_read_b64_tr_b16 v[212:213], v169 offset:0x1600
	ds_read_b64_tr_b16 v[214:215], v169 offset:0x1e00
	v_mfma_f32_32x32x16_bf16 v[32:47], v[194:197], v[218:221], v[32:47]
	ds_read_b64_tr_b16 v[218:219], v169 offset:0x2600
	ds_read_b64_tr_b16 v[220:221], v169 offset:0x2e00
	v_mfma_f32_32x32x16_bf16 v[32:47], v[198:201], v[222:225], v[32:47]
	ds_read_b64_tr_b16 v[222:223], v169 offset:0x3600
	ds_read_b64_tr_b16 v[224:225], v169 offset:0x3e00
	s_waitcnt lgkmcnt(0)
	v_mfma_f32_32x32x16_bf16 v[16:31], v[204:207], v[208:211], v[16:31]
	v_max_f32_e32 v189, v81, v81
	s_barrier
	s_waitcnt vmcnt(0)
	s_waitcnt vmcnt(3)
	ds_write_b128 v173, v[130:133]
	s_waitcnt vmcnt(1)
	ds_write_b128 v174, v[142:145]
	ds_write_b128 v175, v[134:137] offset:32768
	s_waitcnt vmcnt(0)
	ds_write_b128 v176, v[138:141] offset:32768
	v_mfma_f32_32x32x16_bf16 v[16:31], v[190:193], v[212:215], v[16:31]
	v_max_f32_e32 v190, v80, v80
	v_max_f32_e32 v189, v190, v189
	v_max3_f32 v189, v189, v82, v83
	v_max3_f32 v189, v189, v84, v85
	v_max3_f32 v189, v189, v86, v87
	v_max3_f32 v189, v189, v88, v89
	v_max3_f32 v189, v189, v90, v91
	v_max3_f32 v189, v189, v92, v93
	v_max3_f32 v189, v189, v94, v95
	v_max3_f32 v189, v189, v64, v65
	v_max3_f32 v189, v189, v66, v67
	v_max3_f32 v189, v189, v68, v69
	v_max3_f32 v189, v189, v70, v71
	v_max3_f32 v189, v189, v72, v73
	v_max3_f32 v189, v189, v74, v75
	v_max3_f32 v189, v189, v76, v77
	v_mfma_f32_32x32x16_bf16 v[16:31], v[194:197], v[218:221], v[16:31]
	v_max3_f32 v189, v189, v78, v79
	v_mov_b32_e32 v190, v189
	s_nop 1
	v_permlane32_swap_b32_e32 v189, v190
	v_max_f32_e32 v190, v190, v190
	v_max_f32_e32 v189, v189, v189
	v_max_f32_e32 v189, v189, v190
	v_sub_f32_e32 v190, v189, v186
	v_cmp_ge_f32_e32 vcc, s73, v190
	v_max_f32_e32 v190, v186, v186
	v_max_f32_e32 v189, v190, v189
	v_mfma_f32_32x32x16_bf16 v[16:31], v[198:201], v[222:225], v[16:31]
	v_sub_f32_e32 v190, v186, v189
	v_mul_f32_e32 v190, 0x3e0293ee, v190
	v_exp_f32_e32 v190, v190
	s_cmp_eq_u64 vcc, exec
	s_cselect_b64 s[4:5], -1, 0
	v_cndmask_b32_e64 v190, v190, 1.0, s[4:5]
	v_cmp_gt_f32_e32 vcc, 1.0, v190
	s_cbranch_vccz .LBB0_850
	s_and_saveexec_b64 s[8:9], s[2:3]
	ds_write_b32 v171, v190 offset:128
	s_or_b64 exec, exec, s[8:9]
	s_waitcnt lgkmcnt(0)
	v_add_u32_e32 v142, v168, v170
	ds_read_b128 v[130:133], v142 offset:224
	ds_read_b128 v[134:137], v142 offset:192
	ds_read_b128 v[138:141], v142 offset:160
	ds_read_b128 v[142:145], v142 offset:128
	s_waitcnt lgkmcnt(3)
	v_pk_mul_f32 v[12:13], v[12:13], v[130:131]
	s_waitcnt lgkmcnt(2)
	v_pk_mul_f32 v[8:9], v[8:9], v[134:135]
	s_waitcnt lgkmcnt(1)
	v_pk_mul_f32 v[4:5], v[4:5], v[138:139]
	v_pk_mul_f32 v[14:15], v[14:15], v[132:133]
	v_pk_mul_f32 v[10:11], v[10:11], v[136:137]
	v_pk_mul_f32 v[6:7], v[6:7], v[140:141]
	s_waitcnt lgkmcnt(0)
	v_pk_mul_f32 v[2:3], v[2:3], v[144:145]
	v_pk_mul_f32 v[0:1], v[0:1], v[142:143]
	v_pk_mul_f32 v[60:61], v[60:61], v[130:131]
	v_pk_mul_f32 v[56:57], v[56:57], v[134:135]
	v_pk_mul_f32 v[52:53], v[52:53], v[138:139]
	v_pk_mul_f32 v[62:63], v[62:63], v[132:133]
	v_pk_mul_f32 v[58:59], v[58:59], v[136:137]
	v_pk_mul_f32 v[54:55], v[54:55], v[140:141]
	v_pk_mul_f32 v[50:51], v[50:51], v[144:145]
	v_pk_mul_f32 v[48:49], v[48:49], v[142:143]
	v_pk_mul_f32 v[44:45], v[44:45], v[130:131]
	v_pk_mul_f32 v[40:41], v[40:41], v[134:135]
	v_pk_mul_f32 v[36:37], v[36:37], v[138:139]
	v_pk_mul_f32 v[46:47], v[46:47], v[132:133]
	v_pk_mul_f32 v[42:43], v[42:43], v[136:137]
	v_pk_mul_f32 v[38:39], v[38:39], v[140:141]
	v_pk_mul_f32 v[34:35], v[34:35], v[144:145]
	v_pk_mul_f32 v[32:33], v[32:33], v[142:143]
	v_pk_mul_f32 v[28:29], v[28:29], v[130:131]
	v_pk_mul_f32 v[24:25], v[24:25], v[134:135]
	v_pk_mul_f32 v[20:21], v[20:21], v[138:139]
	v_pk_mul_f32 v[30:31], v[30:31], v[132:133]
	v_pk_mul_f32 v[26:27], v[26:27], v[136:137]
	v_pk_mul_f32 v[22:23], v[22:23], v[140:141]
	v_pk_mul_f32 v[18:19], v[18:19], v[144:145]
	v_pk_mul_f32 v[16:17], v[16:17], v[142:143]
.LBB0_850:
	v_cndmask_b32_e64 v186, v189, v186, s[4:5]
	v_mul_f32_e32 v189, 0xbe0293ee, v186
	v_fmamk_f32 v80, v80, 0x3e0293ee, v189
	v_fmamk_f32 v81, v81, 0x3e0293ee, v189
	v_fmamk_f32 v82, v82, 0x3e0293ee, v189
	v_fmamk_f32 v83, v83, 0x3e0293ee, v189
	v_fmamk_f32 v84, v84, 0x3e0293ee, v189
	v_fmamk_f32 v85, v85, 0x3e0293ee, v189
	v_fmamk_f32 v86, v86, 0x3e0293ee, v189
	v_fmamk_f32 v87, v87, 0x3e0293ee, v189
	v_fmamk_f32 v88, v88, 0x3e0293ee, v189
	v_fmamk_f32 v89, v89, 0x3e0293ee, v189
	v_fmamk_f32 v90, v90, 0x3e0293ee, v189
	v_fmamk_f32 v91, v91, 0x3e0293ee, v189
	v_fmamk_f32 v92, v92, 0x3e0293ee, v189
	v_fmamk_f32 v93, v93, 0x3e0293ee, v189
	v_fmamk_f32 v94, v94, 0x3e0293ee, v189
	v_fmamk_f32 v95, v95, 0x3e0293ee, v189
	v_fmamk_f32 v199, v64, 0x3e0293ee, v189
	v_fmamk_f32 v200, v65, 0x3e0293ee, v189
	v_fmamk_f32 v201, v66, 0x3e0293ee, v189
	v_fmamk_f32 v202, v67, 0x3e0293ee, v189
	v_fmamk_f32 v203, v68, 0x3e0293ee, v189
	v_fmamk_f32 v192, v69, 0x3e0293ee, v189
	v_fmamk_f32 v193, v70, 0x3e0293ee, v189
	v_fmamk_f32 v194, v71, 0x3e0293ee, v189
	v_fmamk_f32 v195, v72, 0x3e0293ee, v189
	v_fmamk_f32 v196, v73, 0x3e0293ee, v189
	v_fmamk_f32 v197, v74, 0x3e0293ee, v189
	v_fmamk_f32 v198, v75, 0x3e0293ee, v189
	v_fmamk_f32 v191, v76, 0x3e0293ee, v189
	v_fmamk_f32 v221, v77, 0x3e0293ee, v189
	v_fmamk_f32 v222, v78, 0x3e0293ee, v189
	v_fmac_f32_e32 v189, 0x3e0293ee, v79
	v_exp_f32_e32 v139, v80
	v_exp_f32_e32 v141, v81
	v_exp_f32_e32 v142, v82
	v_exp_f32_e32 v143, v83
	v_exp_f32_e32 v144, v84
	v_exp_f32_e32 v145, v85
	v_exp_f32_e32 v138, v86
	v_exp_f32_e32 v140, v87
	v_exp_f32_e32 v133, v88
	v_exp_f32_e32 v135, v89
	v_exp_f32_e32 v136, v90
	v_exp_f32_e32 v137, v91
	v_exp_f32_e32 v130, v92
	v_exp_f32_e32 v131, v93
	v_exp_f32_e32 v132, v94
	v_exp_f32_e32 v134, v95
	s_waitcnt lgkmcnt(0)
	s_barrier
	ds_read_b128 v[64:67], v177 offset:32768
	ds_read_b128 v[68:71], v177 offset:40960
	ds_read_b128 v[204:207], v178 offset:32768
	ds_read_b128 v[208:211], v178 offset:40960
	ds_read_b128 v[230:233], v179 offset:32768
	ds_read_b128 v[234:237], v179 offset:40960
	ds_read_b128 v[238:241], v180 offset:32768
	ds_read_b128 v[242:245], v180 offset:40960
	v_exp_f32_e32 v215, v191
	v_add_f32_e32 v191, 0, v139
	s_waitcnt lgkmcnt(7)
	v_mfma_f32_32x32x16_bf16 v[80:95], v[64:67], v[126:129], 0
	v_add_f32_e32 v191, v141, v191
	v_add_f32_e32 v191, v142, v191
	v_add_f32_e32 v191, v143, v191
	v_add_f32_e32 v191, v144, v191
	v_add_f32_e32 v191, v145, v191
	v_add_f32_e32 v191, v138, v191
	v_add_f32_e32 v191, v140, v191
	s_waitcnt lgkmcnt(6)
	v_mfma_f32_32x32x16_bf16 v[64:79], v[68:71], v[126:129], 0
	v_add_f32_e32 v191, v133, v191
	v_add_f32_e32 v191, v135, v191
	v_add_f32_e32 v191, v136, v191
	v_add_f32_e32 v191, v137, v191
	v_add_f32_e32 v191, v130, v191
	v_add_f32_e32 v191, v131, v191
	v_add_f32_e32 v191, v132, v191
	s_waitcnt lgkmcnt(5)
	v_mfma_f32_32x32x16_bf16 v[80:95], v[204:207], v[122:125], v[80:95]
	v_add_f32_e32 v191, v134, v191
	v_exp_f32_e32 v193, v193
	v_exp_f32_e32 v212, v196
	v_exp_f32_e32 v213, v197
	v_exp_f32_e32 v214, v198
	v_exp_f32_e32 v218, v221
	v_exp_f32_e32 v219, v222
	s_waitcnt lgkmcnt(4)
	v_mfma_f32_32x32x16_bf16 v[64:79], v[208:211], v[122:125], v[64:79]
	ds_read_b128 v[204:207], v181 offset:32768
	ds_read_b128 v[208:211], v181 offset:40960
	v_exp_f32_e32 v189, v189
	v_cvt_pk_bf16_f32 v196, v144, v145
	v_cvt_pk_bf16_f32 v197, v138, v140
	v_cvt_pk_bf16_f32 v198, v133, v135
	s_waitcnt lgkmcnt(5)
	v_mfma_f32_32x32x16_bf16 v[80:95], v[230:233], v[118:121], v[80:95]
	s_waitcnt lgkmcnt(4)
	v_mfma_f32_32x32x16_bf16 v[64:79], v[234:237], v[118:121], v[64:79]
	ds_read_b128 v[230:233], v182 offset:32768
	ds_read_b128 v[234:237], v182 offset:40960
	s_waitcnt lgkmcnt(5)
	v_mfma_f32_32x32x16_bf16 v[80:95], v[238:241], v[114:117], v[80:95]
	s_waitcnt lgkmcnt(4)
	v_mfma_f32_32x32x16_bf16 v[64:79], v[242:245], v[114:117], v[64:79]
	ds_read_b128 v[238:241], v183 offset:32768
	ds_read_b128 v[242:245], v183 offset:40960
	s_waitcnt lgkmcnt(5)
	v_mfma_f32_32x32x16_bf16 v[80:95], v[204:207], v[110:113], v[80:95]
	s_waitcnt lgkmcnt(4)
	v_mfma_f32_32x32x16_bf16 v[64:79], v[208:211], v[110:113], v[64:79]
	ds_read_b128 v[204:207], v184 offset:32768
	ds_read_b128 v[208:211], v184 offset:40960
	s_waitcnt lgkmcnt(5)
	v_mfma_f32_32x32x16_bf16 v[80:95], v[230:233], v[106:109], v[80:95]
	s_waitcnt lgkmcnt(4)
	v_mfma_f32_32x32x16_bf16 v[64:79], v[234:237], v[106:109], v[64:79]
	s_waitcnt lgkmcnt(3)
	v_mfma_f32_32x32x16_bf16 v[80:95], v[238:241], v[102:105], v[80:95]
	s_waitcnt lgkmcnt(2)
	v_mfma_f32_32x32x16_bf16 v[64:79], v[242:245], v[102:105], v[64:79]
	s_waitcnt lgkmcnt(1)
	v_mfma_f32_32x32x16_bf16 v[80:95], v[204:207], v[98:101], v[80:95]
	v_exp_f32_e32 v204, v199
	v_exp_f32_e32 v205, v200
	v_exp_f32_e32 v206, v201
	v_exp_f32_e32 v207, v202
	v_add_f32_e32 v191, v204, v191
	v_add_f32_e32 v191, v205, v191
	v_add_f32_e32 v191, v206, v191
	s_waitcnt lgkmcnt(0)
	v_mfma_f32_32x32x16_bf16 v[64:79], v[208:211], v[98:101], v[64:79]
	v_exp_f32_e32 v208, v203
	v_exp_f32_e32 v209, v192
	v_exp_f32_e32 v210, v194
	v_add_f32_e32 v191, v207, v191
	v_exp_f32_e32 v211, v195
	v_add_f32_e32 v191, v208, v191
	v_add_f32_e32 v191, v209, v191
	v_add_f32_e32 v191, v193, v191
	v_add_f32_e32 v191, v210, v191
	v_add_f32_e32 v191, v211, v191
	v_add_f32_e32 v191, v212, v191
	v_add_f32_e32 v191, v213, v191
	v_add_f32_e32 v191, v214, v191
	v_add_f32_e32 v191, v215, v191
	v_add_f32_e32 v191, v218, v191
	v_add_f32_e32 v191, v219, v191
	v_add_f32_e32 v191, v189, v191
	v_mov_b32_e32 v192, v191
	s_nop 1
	v_permlane32_swap_b32_e32 v191, v192
	v_cvt_pk_bf16_f32 v194, v139, v141
	v_cvt_pk_bf16_f32 v195, v142, v143
	v_cvt_pk_bf16_f32 v199, v136, v137
	v_cvt_pk_bf16_f32 v200, v130, v131
	v_cvt_pk_bf16_f32 v201, v132, v134
	v_cvt_pk_bf16_f32 v202, v204, v205
	v_cvt_pk_bf16_f32 v203, v206, v207
	v_cvt_pk_bf16_f32 v204, v208, v209
	v_cvt_pk_bf16_f32 v205, v193, v210
	v_cvt_pk_bf16_f32 v206, v211, v212
	v_cvt_pk_bf16_f32 v207, v213, v214
	v_cvt_pk_bf16_f32 v208, v215, v218
	v_cvt_pk_bf16_f32 v209, v219, v189
	v_permlane32_swap_b32_e32 v194, v196
	v_permlane32_swap_b32_e32 v195, v197
	v_permlane32_swap_b32_e32 v198, v200
	v_permlane32_swap_b32_e32 v199, v201
	v_permlane32_swap_b32_e32 v202, v204
	v_permlane32_swap_b32_e32 v203, v205
	v_permlane32_swap_b32_e32 v206, v208
	v_permlane32_swap_b32_e32 v207, v209
	v_add_co_u32_e32 v134, vcc, s49, v166
	s_nop 1
	v_addc_co_u32_e32 v135, vcc, 0, v167, vcc
	v_add_co_u32_e32 v138, vcc, s64, v166
	s_nop 1
	v_addc_co_u32_e32 v139, vcc, 0, v167, vcc
	global_load_dwordx4 v[130:133], v[134:135], off offset:512
	s_nop 0
	global_load_dwordx4 v[134:137], v[134:135], off
	s_nop 0
	global_load_dwordx4 v[142:145], v[138:139], off offset:512
	s_nop 0
	global_load_dwordx4 v[138:141], v[138:139], off
	ds_read_b64_tr_b16 v[210:211], v172 offset:0
	ds_read_b64_tr_b16 v[212:213], v172 offset:0x800
	ds_read_b64_tr_b16 v[218:219], v172 offset:0x1000
	ds_read_b64_tr_b16 v[220:221], v172 offset:0x1800
	ds_read_b64_tr_b16 v[222:223], v172 offset:0x2000
	ds_read_b64_tr_b16 v[224:225], v172 offset:0x2800
	ds_read_b64_tr_b16 v[226:227], v172 offset:0x3000
	ds_read_b64_tr_b16 v[228:229], v172 offset:0x3800
	s_waitcnt lgkmcnt(0)
	s_nop 0
	v_mfma_f32_32x32x16_bf16 v[0:15], v[194:197], v[210:213], v[0:15]
	ds_read_b64_tr_b16 v[210:211], v172 offset:0x200
	ds_read_b64_tr_b16 v[212:213], v172 offset:0xa00
	v_mfma_f32_32x32x16_bf16 v[0:15], v[198:201], v[218:221], v[0:15]
	ds_read_b64_tr_b16 v[218:219], v172 offset:0x1200
	ds_read_b64_tr_b16 v[220:221], v172 offset:0x1a00
	v_mfma_f32_32x32x16_bf16 v[0:15], v[202:205], v[222:225], v[0:15]
	ds_read_b64_tr_b16 v[222:223], v172 offset:0x2200
	ds_read_b64_tr_b16 v[224:225], v172 offset:0x2a00
	v_mfma_f32_32x32x16_bf16 v[0:15], v[206:209], v[226:229], v[0:15]
	ds_read_b64_tr_b16 v[226:227], v172 offset:0x3200
	ds_read_b64_tr_b16 v[228:229], v172 offset:0x3a00
	s_waitcnt lgkmcnt(0)
	v_mfma_f32_32x32x16_bf16 v[48:63], v[194:197], v[210:213], v[48:63]
	ds_read_b64_tr_b16 v[210:211], v172 offset:0x400
	ds_read_b64_tr_b16 v[212:213], v172 offset:0xc00
	v_mfma_f32_32x32x16_bf16 v[48:63], v[198:201], v[218:221], v[48:63]
	ds_read_b64_tr_b16 v[218:219], v172 offset:0x1400
	ds_read_b64_tr_b16 v[220:221], v172 offset:0x1c00
	v_mfma_f32_32x32x16_bf16 v[48:63], v[202:205], v[222:225], v[48:63]
	ds_read_b64_tr_b16 v[222:223], v172 offset:0x2400
	ds_read_b64_tr_b16 v[224:225], v172 offset:0x2c00
	v_mfma_f32_32x32x16_bf16 v[48:63], v[206:209], v[226:229], v[48:63]
	ds_read_b64_tr_b16 v[226:227], v172 offset:0x3400
	ds_read_b64_tr_b16 v[228:229], v172 offset:0x3c00
	s_waitcnt lgkmcnt(0)
	v_mfma_f32_32x32x16_bf16 v[32:47], v[194:197], v[210:213], v[32:47]
	ds_read_b64_tr_b16 v[210:211], v172 offset:0x600
	ds_read_b64_tr_b16 v[212:213], v172 offset:0xe00
	v_mfma_f32_32x32x16_bf16 v[32:47], v[198:201], v[218:221], v[32:47]
	ds_read_b64_tr_b16 v[218:219], v172 offset:0x1600
	ds_read_b64_tr_b16 v[220:221], v172 offset:0x1e00
	v_mfma_f32_32x32x16_bf16 v[32:47], v[202:205], v[222:225], v[32:47]
	ds_read_b64_tr_b16 v[222:223], v172 offset:0x2600
	ds_read_b64_tr_b16 v[224:225], v172 offset:0x2e00
	v_mfma_f32_32x32x16_bf16 v[32:47], v[206:209], v[226:229], v[32:47]
	ds_read_b64_tr_b16 v[226:227], v172 offset:0x3600
	ds_read_b64_tr_b16 v[228:229], v172 offset:0x3e00
	s_waitcnt lgkmcnt(0)
	v_mfma_f32_32x32x16_bf16 v[16:31], v[194:197], v[210:213], v[16:31]
	v_max_f32_e32 v189, v81, v81
	v_max_f32_e32 v193, v80, v80
	v_max_f32_e32 v189, v193, v189
	v_max3_f32 v189, v189, v82, v83
	v_max3_f32 v189, v189, v84, v85
	v_max3_f32 v189, v189, v86, v87
	v_max3_f32 v189, v189, v88, v89
	v_max3_f32 v189, v189, v90, v91
	v_max3_f32 v189, v189, v92, v93
	v_mfma_f32_32x32x16_bf16 v[16:31], v[198:201], v[218:221], v[16:31]
	v_max3_f32 v189, v189, v94, v95
	v_max3_f32 v189, v189, v64, v65
	v_max3_f32 v189, v189, v66, v67
	v_max3_f32 v189, v189, v68, v69
	v_max3_f32 v189, v189, v70, v71
	v_max3_f32 v189, v189, v72, v73
	v_max3_f32 v189, v189, v74, v75
	v_max3_f32 v189, v189, v76, v77
	v_mfma_f32_32x32x16_bf16 v[16:31], v[202:205], v[222:225], v[16:31]
	v_max3_f32 v189, v189, v78, v79
	v_mov_b32_e32 v193, v189
	s_nop 1
	v_permlane32_swap_b32_e32 v189, v193
	v_max_f32_e32 v193, v193, v193
	v_max_f32_e32 v189, v189, v189
	v_max_f32_e32 v189, v189, v193
	v_sub_f32_e32 v193, v189, v186
	v_cmp_ge_f32_e32 vcc, s73, v193
	v_max_f32_e32 v193, v186, v186
	v_max_f32_e32 v193, v193, v189
	v_mfma_f32_32x32x16_bf16 v[16:31], v[206:209], v[226:229], v[16:31]
	v_sub_f32_e32 v189, v186, v193
	v_mul_f32_e32 v189, 0x3e0293ee, v189
	v_exp_f32_e32 v189, v189
	s_cmp_eq_u64 vcc, exec
	s_cselect_b64 s[4:5], -1, 0
	s_barrier
	s_waitcnt vmcnt(0)
	v_cndmask_b32_e64 v189, v189, 1.0, s[4:5]
	v_cmp_gt_f32_e32 vcc, 1.0, v189
	s_waitcnt vmcnt(3)
	ds_write_b128 v173, v[130:133] offset:16384
	s_waitcnt vmcnt(1)
	ds_write_b128 v174, v[142:145] offset:16384
	ds_write_b128 v175, v[134:137] offset:49152
	s_waitcnt vmcnt(0)
	ds_write_b128 v176, v[138:141] offset:49152
	s_cbranch_vccz .LBB0_854
	s_and_saveexec_b64 s[8:9], s[2:3]
	ds_write_b32 v171, v189 offset:128
	s_or_b64 exec, exec, s[8:9]
	s_waitcnt lgkmcnt(0)
	v_add_u32_e32 v142, v168, v170
	ds_read_b128 v[130:133], v142 offset:224
	ds_read_b128 v[134:137], v142 offset:192
	ds_read_b128 v[138:141], v142 offset:160
	ds_read_b128 v[142:145], v142 offset:128
	s_waitcnt lgkmcnt(3)
	v_pk_mul_f32 v[12:13], v[12:13], v[130:131]
	s_waitcnt lgkmcnt(2)
	v_pk_mul_f32 v[8:9], v[8:9], v[134:135]
	s_waitcnt lgkmcnt(1)
	v_pk_mul_f32 v[4:5], v[4:5], v[138:139]
	v_pk_mul_f32 v[14:15], v[14:15], v[132:133]
	v_pk_mul_f32 v[10:11], v[10:11], v[136:137]
	v_pk_mul_f32 v[6:7], v[6:7], v[140:141]
	s_waitcnt lgkmcnt(0)
	v_pk_mul_f32 v[2:3], v[2:3], v[144:145]
	v_pk_mul_f32 v[0:1], v[0:1], v[142:143]
	v_pk_mul_f32 v[60:61], v[60:61], v[130:131]
	v_pk_mul_f32 v[56:57], v[56:57], v[134:135]
	v_pk_mul_f32 v[52:53], v[52:53], v[138:139]
	v_pk_mul_f32 v[62:63], v[62:63], v[132:133]
	v_pk_mul_f32 v[58:59], v[58:59], v[136:137]
	v_pk_mul_f32 v[54:55], v[54:55], v[140:141]
	v_pk_mul_f32 v[50:51], v[50:51], v[144:145]
	v_pk_mul_f32 v[48:49], v[48:49], v[142:143]
	v_pk_mul_f32 v[44:45], v[44:45], v[130:131]
	v_pk_mul_f32 v[40:41], v[40:41], v[134:135]
	v_pk_mul_f32 v[36:37], v[36:37], v[138:139]
	v_pk_mul_f32 v[46:47], v[46:47], v[132:133]
	v_pk_mul_f32 v[42:43], v[42:43], v[136:137]
	v_pk_mul_f32 v[38:39], v[38:39], v[140:141]
	v_pk_mul_f32 v[34:35], v[34:35], v[144:145]
	v_pk_mul_f32 v[32:33], v[32:33], v[142:143]
	v_pk_mul_f32 v[28:29], v[28:29], v[130:131]
	v_pk_mul_f32 v[24:25], v[24:25], v[134:135]
	v_pk_mul_f32 v[20:21], v[20:21], v[138:139]
	v_pk_mul_f32 v[30:31], v[30:31], v[132:133]
	v_pk_mul_f32 v[26:27], v[26:27], v[136:137]
	v_pk_mul_f32 v[22:23], v[22:23], v[140:141]
	v_pk_mul_f32 v[18:19], v[18:19], v[144:145]
	v_pk_mul_f32 v[16:17], v[16:17], v[142:143]
